# w1[l] converted in phase D of the same layer and w2[l] in expert GEMM 1 of the same layer for all four layers; the prologue converts no expert weights any more
# speedup vs baseline: 1.0229x; 1.0172x over previous
.LBB0_10:
	s_cmpk_gt_i32 s73, 0x9ff
	s_mov_b64 s[4:5], -1
	s_cbranch_scc0 .LBB0_89
	s_cmpk_gt_u32 s73, 0x1dff
	s_cbranch_scc0 .LBB0_21
	s_cmpk_gt_u32 s73, 0x21ff
	s_cbranch_scc0 .LBB0_18
	s_cmp_gt_u32 s73, 0x121ff
	s_cbranch_scc0 .LBB0_15
	s_cmpk_lg_i32 s16, 0x800
	s_cbranch_scc1 .Lp0_w2_do
	s_cmp_gt_u32 s73, 0x121ff
	s_cbranch_scc1 .Lp0_w2_skip

.LBB0_15:
	s_andn2_b64 vcc, exec, s[4:5]
	s_cbranch_vccnz .LBB0_17
	s_cmpk_lg_i32 s16, 0x800
	s_cbranch_scc1 .Lp0_w1_do
	s_cmp_gt_u32 s73, 0x21ff
	s_cbranch_scc1 .LBB0_17

.LBB0_623:
	v_mul_lo_u32 v50, v176, s69
	v_add_u32_e32 v158, s53, v50
	v_and_b32_e32 v179, -16, v175
	v_add_u32_e32 v50, v158, v179
	v_mul_u32_u24_e32 v51, 0x48, v106
	s_waitcnt lgkmcnt(0)
	s_barrier
	s_cmpk_lg_i32 s29, 0x100
	s_cbranch_scc1 .Lcv_skip_i0
	s_cmp_gt_u32 s74, 3
	s_cbranch_scc1 .Lcv_skip_i0
	s_load_dwordx2 s[60:61], s[0:1], 0x68
	s_load_dwordx2 s[62:63], s[0:1], 0xa0
	v_readfirstlane_b32 s87, v0
	s_lshr_b32 s87, s87, 6
	s_lshl_b32 s88, s2, 3
	s_add_i32 s88, s88, s87
	s_lshr_b32 s96, s75, 8
	s_lshl_b32 s96, s96, 1
	s_lshl_b32 s96, s96, 11
	s_add_i32 s96, s96, s88
	s_lshr_b32 s51, s96, 10
	s_add_i32 s32, s74, 0
	s_lshl_b32 s32, s32, 5
	s_add_i32 s51, s51, s32
	s_bfe_u32 s32, s96, 0x30007
	s_and_b32 s33, s96, 0x7f
	s_lshl_b32 s92, s51, 23
	s_lshl_b32 s93, s32, 20
	s_add_u32 s92, s92, s93
	s_lshl_b32 s93, s33, 6
	s_add_u32 s96, s92, s93
	s_and_b32 s92, s33, 63
	s_lshr_b32 s92, s92, 3
	s_lshl_b32 s92, s92, 8
	s_lshr_b32 s93, s33, 6
	s_lshl_b32 s93, s93, 7
	s_or_b32 s92, s92, s93
	s_and_b32 s93, s33, 7
	s_lshl_b32 s93, s93, 4
	s_or_b32 s92, s92, s93
	s_lshl_b32 s92, s92, 10
	s_lshl_b32 s93, s32, 7
	s_add_u32 s92, s92, s93
	s_lshl_b32 s93, s51, 21
	s_add_u32 s92, s92, s93
	s_add_u32 s92, s92, 0x1f00000
	s_waitcnt lgkmcnt(0)
	s_add_u32 s60, s60, s96
	s_addc_u32 s61, s61, 0
	s_add_u32 s62, s62, s92
	s_addc_u32 s63, s63, 0
	v_and_b32_e32 v195, 63, v0
	v_lshrrev_b32_e32 v196, 2, v195
	v_and_b32_e32 v195, 3, v195
	v_lshlrev_b32_e32 v196, 15, v196
	v_lshl_or_b32 v195, v195, 4, v196
	global_load_dwordx4 v[202:205], v195, s[60:61]
	v_add_u32_e32 v196, 0x2000, v195
	global_load_dwordx4 v[206:209], v196, s[60:61]
	v_add_u32_e32 v196, 0x4000, v195
	global_load_dwordx4 v[210:213], v196, s[60:61]
	v_add_u32_e32 v196, 0x6000, v195
	global_load_dwordx4 v[216:219], v196, s[60:61]
	v_add_u32_e32 v196, 0x80000, v195
	global_load_dwordx4 v[220:223], v196, s[60:61]
	v_add_u32_e32 v196, 0x82000, v195
	global_load_dwordx4 v[224:227], v196, s[60:61]
	v_add_u32_e32 v196, 0x84000, v195
	global_load_dwordx4 v[228:231], v196, s[60:61]
	v_add_u32_e32 v196, 0x86000, v195
	global_load_dwordx4 v[246:249], v196, s[60:61]

.LBB0_701:
	s_cmpk_lg_i32 s29, 0x100
	s_cbranch_scc1 .Lcv_skip_f0
	s_cmp_gt_u32 s74, 3
	s_cbranch_scc1 .Lcv_skip_f0
	s_waitcnt vmcnt(0)
	s_mov_b32 s32, 0x42000000
	s_mov_b32 s33, 0x42000000
	v_pk_mul_f32 v[202:203], v[202:203], s[32:33]
	v_pk_mul_f32 v[204:205], v[204:205], s[32:33]
	v_pk_mul_f32 v[206:207], v[206:207], s[32:33]
	v_pk_mul_f32 v[208:209], v[208:209], s[32:33]
	v_pk_mul_f32 v[210:211], v[210:211], s[32:33]
	v_pk_mul_f32 v[212:213], v[212:213], s[32:33]
	v_pk_mul_f32 v[216:217], v[216:217], s[32:33]
	v_pk_mul_f32 v[218:219], v[218:219], s[32:33]
	v_pk_mul_f32 v[220:221], v[220:221], s[32:33]
	v_pk_mul_f32 v[222:223], v[222:223], s[32:33]
	v_pk_mul_f32 v[224:225], v[224:225], s[32:33]
	v_pk_mul_f32 v[226:227], v[226:227], s[32:33]
	v_pk_mul_f32 v[228:229], v[228:229], s[32:33]
	v_pk_mul_f32 v[230:231], v[230:231], s[32:33]
	v_pk_mul_f32 v[246:247], v[246:247], s[32:33]
	v_pk_mul_f32 v[248:249], v[248:249], s[32:33]
	v_cvt_pk_fp8_f32 v202, v202, v206
	v_cvt_pk_fp8_f32 v202, v210, v216 op_sel:[0,0,1]
	v_cvt_pk_fp8_f32 v203, v203, v207
	v_cvt_pk_fp8_f32 v203, v211, v217 op_sel:[0,0,1]
	v_cvt_pk_fp8_f32 v204, v204, v208
	v_cvt_pk_fp8_f32 v204, v212, v218 op_sel:[0,0,1]
	v_cvt_pk_fp8_f32 v205, v205, v209
	v_cvt_pk_fp8_f32 v205, v213, v219 op_sel:[0,0,1]
	v_cvt_pk_fp8_f32 v220, v220, v224
	v_cvt_pk_fp8_f32 v220, v228, v246 op_sel:[0,0,1]
	v_cvt_pk_fp8_f32 v221, v221, v225
	v_cvt_pk_fp8_f32 v221, v229, v247 op_sel:[0,0,1]
	v_cvt_pk_fp8_f32 v222, v222, v226
	v_cvt_pk_fp8_f32 v222, v230, v248 op_sel:[0,0,1]
	v_cvt_pk_fp8_f32 v223, v223, v227
	v_cvt_pk_fp8_f32 v223, v231, v249 op_sel:[0,0,1]
	v_readfirstlane_b32 s87, v0
	s_lshr_b32 s87, s87, 6
	s_mul_i32 s87, s87, 0x840
	s_add_i32 s88, s53, 0x22000
	s_add_i32 s88, s88, s87
	v_and_b32_e32 v250, 63, v0
	v_and_b32_e32 v251, 3, v250
	v_mul_u32_u24_e32 v251, 0x84, v251
	v_lshrrev_b32_e32 v252, 2, v250
	v_add_u32_e32 v251, v251, v252
	v_lshl_add_u32 v251, v251, 2, s88
	ds_write2_b32 v251, v202, v220 offset0:0 offset1:16
	ds_write2_b32 v251, v203, v221 offset0:33 offset1:49
	ds_write2_b32 v251, v204, v222 offset0:66 offset1:82
	ds_write2_b32 v251, v205, v223 offset0:99 offset1:115
	v_lshrrev_b32_e32 v252, 3, v250
	v_mul_u32_u24_e32 v252, 33, v252
	v_and_b32_e32 v253, 7, v250
	v_lshl_add_u32 v252, v253, 2, v252
	v_lshl_add_u32 v252, v252, 2, s88
	v_add_u32_e32 v243, 0x420, v252
	v_lshrrev_b32_e32 v251, 3, v250
	v_lshlrev_b32_e32 v251, 10, v251
	v_lshl_or_b32 v251, v253, 4, v251
	v_add_u32_e32 v253, 0x2000, v251
	s_waitcnt lgkmcnt(0)
	ds_read2_b32 v[202:203], v252 offset1:1
	ds_read2_b32 v[204:205], v252 offset0:2 offset1:3
	ds_read2_b32 v[206:207], v243 offset1:1
	ds_read2_b32 v[208:209], v243 offset0:2 offset1:3
	s_waitcnt lgkmcnt(0)
	global_store_dwordx4 v251, v[202:205], s[62:63] sc1 nt
	global_store_dwordx4 v253, v[206:209], s[62:63] sc1 nt
.Lcv_skip_f0:
	s_cmpk_lg_i32 s29, 0x100
	s_cbranch_scc1 .Lcv_skip_i1
	s_cmp_gt_u32 s74, 3
	s_cbranch_scc1 .Lcv_skip_i1
	s_load_dwordx2 s[60:61], s[0:1], 0x68
	s_load_dwordx2 s[62:63], s[0:1], 0xa0
	v_readfirstlane_b32 s87, v0
	s_lshr_b32 s87, s87, 6
	s_lshl_b32 s88, s2, 3
	s_add_i32 s88, s88, s87
	s_lshr_b32 s96, s75, 8
	s_lshl_b32 s96, s96, 1
	s_add_i32 s96, s96, 1
	s_lshl_b32 s96, s96, 11
	s_add_i32 s96, s96, s88
	s_lshr_b32 s51, s96, 10
	s_add_i32 s32, s74, 0
	s_lshl_b32 s32, s32, 5
	s_add_i32 s51, s51, s32
	s_bfe_u32 s32, s96, 0x30007
	s_and_b32 s33, s96, 0x7f
	s_lshl_b32 s92, s51, 23
	s_lshl_b32 s93, s32, 20
	s_add_u32 s92, s92, s93
	s_lshl_b32 s93, s33, 6
	s_add_u32 s96, s92, s93
	s_and_b32 s92, s33, 63
	s_lshr_b32 s92, s92, 3
	s_lshl_b32 s92, s92, 8
	s_lshr_b32 s93, s33, 6
	s_lshl_b32 s93, s93, 7
	s_or_b32 s92, s92, s93
	s_and_b32 s93, s33, 7
	s_lshl_b32 s93, s93, 4
	s_or_b32 s92, s92, s93
	s_lshl_b32 s92, s92, 10
	s_lshl_b32 s93, s32, 7
	s_add_u32 s92, s92, s93
	s_lshl_b32 s93, s51, 21
	s_add_u32 s92, s92, s93
	s_add_u32 s92, s92, 0x1f00000
	s_waitcnt lgkmcnt(0)
	s_add_u32 s60, s60, s96
	s_addc_u32 s61, s61, 0
	s_add_u32 s62, s62, s92
	s_addc_u32 s63, s63, 0
	v_and_b32_e32 v195, 63, v0
	v_lshrrev_b32_e32 v196, 2, v195
	v_and_b32_e32 v195, 3, v195
	v_lshlrev_b32_e32 v196, 15, v196
	v_lshl_or_b32 v195, v195, 4, v196
	global_load_dwordx4 v[202:205], v195, s[60:61]
	v_add_u32_e32 v196, 0x2000, v195
	global_load_dwordx4 v[206:209], v196, s[60:61]
	v_add_u32_e32 v196, 0x4000, v195
	global_load_dwordx4 v[210:213], v196, s[60:61]
	v_add_u32_e32 v196, 0x6000, v195
	global_load_dwordx4 v[216:219], v196, s[60:61]
	v_add_u32_e32 v196, 0x80000, v195
	global_load_dwordx4 v[220:223], v196, s[60:61]
	v_add_u32_e32 v196, 0x82000, v195
	global_load_dwordx4 v[224:227], v196, s[60:61]
	v_add_u32_e32 v196, 0x84000, v195
	global_load_dwordx4 v[228:231], v196, s[60:61]
	v_add_u32_e32 v196, 0x86000, v195
	global_load_dwordx4 v[246:249], v196, s[60:61]

.LBB0_1061:
	v_mov_b32_e32 v2, v243
	s_nop 15
	s_nop 15
	s_lshl_b32 s23, s51, 8
	v_readfirstlane_b32 s21, v2
	s_ashr_i32 s25, s21, 2
	s_andn2_b32 s25, s25, 63
	s_lshr_b32 s21, s21, 1
	s_add_i32 s25, s25, s23
	s_lshl_b32 s23, s76, 7
	s_and_b32 s21, s21, 0x60
	v_and_or_b32 v6, v2, 15, s25
	s_or_b32 s21, s21, s23
	v_lshrrev_b32_e32 v2, 1, v2
	v_and_or_b32 v4, v2, 24, s21
	s_waitcnt vmcnt(8)
	s_mov_b32 s32, 0
	s_cmp_gt_u32 s74, 3
	s_cbranch_scc1 .Lcg_skip_i
	s_cmp_gt_u32 s51, 0x1ff
	s_cbranch_scc1 .Lcg_skip_i
	s_load_dword s101, s[0:1], 0xb0
	s_load_dwordx2 s[80:81], s[0:1], 0x78
	s_load_dwordx2 s[82:83], s[0:1], 0xa0
	v_readlane_b32 s84, v255, 7
	v_readfirstlane_b32 s85, v0
	s_lshr_b32 s85, s85, 6
	s_lshl_b32 s84, s84, 3
	s_add_i32 s84, s84, s85
	s_bfe_u32 s85, s51, 0x30006
	s_lshl_b32 s85, s85, 11
	s_add_i32 s85, s85, s84
	s_lshr_b32 s84, s85, 9
	s_add_i32 s92, s74, 0
	s_lshl_b32 s92, s92, 5
	s_add_i32 s84, s84, s92
	s_lshl_b32 s92, s84, 22
	s_bfe_u32 s93, s85, 0x30006
	s_lshl_b32 s93, s93, 19
	s_add_u32 s92, s92, s93
	s_and_b32 s93, s85, 63
	s_lshl_b32 s93, s93, 6
	s_add_u32 s92, s92, s93
	s_bfe_u32 s93, s51, 0x10005
	s_lshl_b32 s93, s93, 18
	s_add_u32 s100, s92, s93
	s_lshl_b32 s92, s84, 20
	s_and_b32 s93, s85, 63
	s_lshl_b32 s93, s93, 14
	s_add_u32 s92, s92, s93
	s_bfe_u32 s93, s85, 0x30006
	s_lshl_b32 s93, s93, 7
	s_add_u32 s92, s92, s93
	s_bfe_u32 s93, s51, 0x10005
	s_lshl_b32 s93, s93, 6
	s_add_u32 s92, s92, s93
	s_add_u32 s92, s92, 0x21f00000
	s_waitcnt lgkmcnt(0)
	s_cmpk_lg_i32 s101, 0x100
	s_cbranch_scc1 .Lcg_skip_i
	s_add_u32 s80, s80, s100
	s_addc_u32 s81, s81, 0
	s_add_u32 s82, s82, s92
	s_addc_u32 s83, s83, 0
	v_and_b32_e32 v56, 63, v0
	v_lshrrev_b32_e32 v57, 2, v56
	v_and_b32_e32 v56, 3, v56
	v_lshlrev_b32_e32 v57, 14, v57
	v_lshl_or_b32 v56, v56, 4, v57
	global_load_dwordx4 v[24:27], v56, s[80:81]
	v_add_u32_e32 v57, 0x1000, v56
	global_load_dwordx4 v[28:31], v57, s[80:81]
	v_add_u32_e32 v57, 0x2000, v56
	global_load_dwordx4 v[32:35], v57, s[80:81]
	v_add_u32_e32 v57, 0x3000, v56
	global_load_dwordx4 v[36:39], v57, s[80:81]
	s_mov_b32 s32, 1
